# speedup vs baseline: 1.0277x; 1.0243x over previous
.Lmy_ffn3_k2:
	ds_read_b128 v[34:37], v195
	ds_read_b128 v[38:41], v195 offset:288
	ds_read_b128 v[42:45], v195 offset:576
	ds_read_b128 v[46:49], v195 offset:864
	ds_read_b128 v[196:199], v194
	ds_read_b128 v[200:203], v194 offset:1024
	ds_read_b128 v[204:207], v194 offset:2048
	ds_read_b128 v[208:211], v194 offset:3072
	v_add_u32_e32 v194, 0x1000, v194
	v_add_u32_e32 v195, 0x480, v195
	s_add_i32 s15, s15, -1
	s_waitcnt lgkmcnt(3)
	v_mfma_f32_32x32x16_f16 v[34:49], v[196:199], v[50:53], v[34:49]
	s_waitcnt lgkmcnt(2)
	v_mfma_f32_32x32x16_f16 v[34:49], v[200:203], v[54:57], v[34:49]
	s_waitcnt lgkmcnt(1)
	v_mfma_f32_32x32x16_f16 v[34:49], v[204:207], v[58:61], v[34:49]
	s_waitcnt lgkmcnt(0)
	v_mfma_f32_32x32x16_f16 v[34:49], v[208:211], v[62:65], v[34:49]
	ds_read_b128 v[100:103], v236 offset:57344
	ds_read_b128 v[186:189], v237
	ds_read_b128 v[112:115], v236 offset:58368
	ds_read_b128 v[190:193], v237 offset:1024
	v_add_u32_e32 v236, 0x800, v236
	v_add_u32_e32 v237, 0x800, v237
	s_cmp_lg_u32 s15, 0
	s_nop 4
	v_max_f32_e32 v34, 0, v34
	v_max_f32_e32 v35, 0, v35
	v_max_f32_e32 v36, 0, v36
	v_max_f32_e32 v37, 0, v37
	v_max_f32_e32 v38, 0, v38
	v_max_f32_e32 v39, 0, v39
	v_max_f32_e32 v40, 0, v40
	v_max_f32_e32 v41, 0, v41
	v_cvt_pkrtz_f16_f32 v34, v34, v35
	v_cvt_pkrtz_f16_f32 v35, v36, v37
	v_cvt_pkrtz_f16_f32 v36, v38, v39
	v_cvt_pkrtz_f16_f32 v37, v40, v41
	s_waitcnt lgkmcnt(2)
	s_nop 0
	v_mfma_f32_32x32x16_f16 v[18:33], v[100:103], v[34:37], v[18:33]
	v_mfma_f32_32x32x16_f16 v[2:17], v[186:189], v[34:37], v[2:17]
	v_max_f32_e32 v42, 0, v42
	v_max_f32_e32 v43, 0, v43
	v_max_f32_e32 v44, 0, v44
	v_max_f32_e32 v45, 0, v45
	v_max_f32_e32 v46, 0, v46
	v_max_f32_e32 v47, 0, v47
	v_max_f32_e32 v48, 0, v48
	v_max_f32_e32 v49, 0, v49
	v_cvt_pkrtz_f16_f32 v34, v42, v43
	v_cvt_pkrtz_f16_f32 v35, v44, v45
	v_cvt_pkrtz_f16_f32 v36, v46, v47
	v_cvt_pkrtz_f16_f32 v37, v48, v49
	s_waitcnt lgkmcnt(0)
	s_nop 0
	v_mfma_f32_32x32x16_f16 v[18:33], v[112:115], v[34:37], v[18:33]
	v_mfma_f32_32x32x16_f16 v[2:17], v[190:193], v[34:37], v[2:17]
	s_cbranch_scc1 .Lmy_ffn3_k2
	ds_read_b128 v[34:37], v173 offset:27776
	ds_read_b128 v[38:41], v173 offset:28064
	ds_read_b128 v[42:45], v173 offset:28352
	ds_read_b128 v[46:49], v173 offset:28640
	ds_read_b128 v[50:53], v173 offset:28928
	ds_read_b128 v[54:57], v173 offset:29216
	ds_read_b128 v[58:61], v173 offset:29504
	ds_read_b128 v[62:65], v173 offset:29792
	ds_read_b128 v[98:101], v173 offset:13952
	ds_read_b128 v[102:105], v173 offset:14240
	ds_read_b128 v[106:109], v173 offset:16256
	ds_read_b128 v[110:113], v173 offset:16544
	ds_read_b128 v[114:117], v173 offset:14528
	ds_read_b128 v[174:177], v173 offset:14816
	ds_read_b128 v[178:181], v173 offset:16832
	ds_read_b128 v[182:185], v173 offset:17120
	s_waitcnt lgkmcnt(14)
	v_pk_add_f32 v[18:19], v[18:19], v[34:35]
	v_pk_add_f32 v[20:21], v[20:21], v[36:37]
	v_pk_add_f32 v[18:19], v[68:69], v[18:19]
	v_pk_add_f32 v[20:21], v[66:67], v[20:21]
	v_add_f32_e32 v34, 0, v18
	v_add_f32_e32 v34, v19, v34
	v_pk_add_f32 v[22:23], v[22:23], v[38:39]
	v_add_f32_e32 v34, v20, v34
	v_pk_add_f32 v[22:23], v[70:71], v[22:23]
	v_add_f32_e32 v34, v21, v34
	v_pk_add_f32 v[24:25], v[24:25], v[40:41]
	v_add_f32_e32 v34, v22, v34
	v_pk_add_f32 v[24:25], v[72:73], v[24:25]
	v_add_f32_e32 v34, v23, v34
	s_waitcnt lgkmcnt(13)
	v_pk_add_f32 v[26:27], v[26:27], v[42:43]
	v_add_f32_e32 v34, v24, v34
	v_pk_add_f32 v[26:27], v[74:75], v[26:27]
	v_add_f32_e32 v34, v25, v34
	v_pk_add_f32 v[28:29], v[28:29], v[44:45]
	v_add_f32_e32 v34, v26, v34
	v_pk_add_f32 v[28:29], v[76:77], v[28:29]
	v_add_f32_e32 v34, v27, v34
	s_waitcnt lgkmcnt(12)
	v_pk_add_f32 v[30:31], v[30:31], v[46:47]
	v_add_f32_e32 v34, v28, v34
	v_pk_add_f32 v[30:31], v[78:79], v[30:31]
	v_add_f32_e32 v34, v29, v34
	v_pk_add_f32 v[32:33], v[32:33], v[48:49]
	v_add_f32_e32 v34, v30, v34
	v_pk_add_f32 v[32:33], v[80:81], v[32:33]
	v_add_f32_e32 v34, v31, v34
	s_waitcnt lgkmcnt(11)
	v_pk_add_f32 v[2:3], v[2:3], v[50:51]
	v_add_f32_e32 v34, v32, v34
	v_pk_add_f32 v[96:97], v[96:97], v[2:3]
	v_add_f32_e32 v34, v33, v34
	v_pk_add_f32 v[2:3], v[4:5], v[52:53]
	v_add_f32_e32 v34, v96, v34
	v_pk_add_f32 v[94:95], v[94:95], v[2:3]
	v_add_f32_e32 v34, v97, v34
	s_waitcnt lgkmcnt(10)
	v_pk_add_f32 v[6:7], v[6:7], v[54:55]
	v_add_f32_e32 v34, v94, v34
	v_pk_add_f32 v[6:7], v[92:93], v[6:7]
	v_add_f32_e32 v34, v95, v34
	v_pk_add_f32 v[8:9], v[8:9], v[56:57]
	v_add_f32_e32 v34, v6, v34
	v_pk_add_f32 v[8:9], v[90:91], v[8:9]
	v_add_f32_e32 v34, v7, v34
	s_waitcnt lgkmcnt(9)
	v_pk_add_f32 v[10:11], v[10:11], v[58:59]
	v_add_f32_e32 v34, v8, v34
	v_pk_add_f32 v[10:11], v[88:89], v[10:11]
	v_add_f32_e32 v34, v9, v34
	v_pk_add_f32 v[12:13], v[12:13], v[60:61]
	v_add_f32_e32 v34, v10, v34
	v_pk_add_f32 v[12:13], v[86:87], v[12:13]
	v_add_f32_e32 v34, v11, v34
	s_waitcnt lgkmcnt(8)
	v_pk_add_f32 v[14:15], v[14:15], v[62:63]
	v_add_f32_e32 v34, v12, v34
	v_pk_add_f32 v[14:15], v[82:83], v[14:15]
	v_add_f32_e32 v34, v13, v34
	v_pk_add_f32 v[16:17], v[16:17], v[64:65]
	v_add_f32_e32 v34, v14, v34
	v_pk_add_f32 v[16:17], v[84:85], v[16:17]
	v_add_f32_e32 v34, v15, v34
	v_add_f32_e32 v34, v16, v34
	v_add_f32_e32 v34, v17, v34
	v_mov_b32_e32 v35, v34
	v_mov_b32_e32 v36, v34
	s_nop 1
	v_permlane32_swap_b32_e32 v35, v36
	v_cndmask_b32_e64 v35, v35, v36, s[2:3]
	v_add_f32_e32 v34, v34, v35
	v_mul_f32_e32 v34, 0x3c800000, v34
	v_pk_add_f32 v[36:37], v[18:19], v[34:35] op_sel_hi:[1,0] neg_lo:[0,1] neg_hi:[0,1]
	v_pk_add_f32 v[38:39], v[20:21], v[34:35] op_sel_hi:[1,0] neg_lo:[0,1] neg_hi:[0,1]
	v_pk_mul_f32 v[18:19], v[36:37], v[36:37]
	v_pk_mul_f32 v[20:21], v[38:39], v[38:39]
	v_add_f32_e32 v18, v18, v19
	v_pk_add_f32 v[22:23], v[22:23], v[34:35] op_sel_hi:[1,0] neg_lo:[0,1] neg_hi:[0,1]
	v_add_f32_e32 v18, v20, v18
	v_pk_mul_f32 v[40:41], v[22:23], v[22:23]
	v_add_f32_e32 v18, v21, v18
	v_pk_add_f32 v[24:25], v[24:25], v[34:35] op_sel_hi:[1,0] neg_lo:[0,1] neg_hi:[0,1]
	v_add_f32_e32 v18, v40, v18
	v_pk_mul_f32 v[42:43], v[24:25], v[24:25]
	v_add_f32_e32 v18, v41, v18
	v_pk_add_f32 v[26:27], v[26:27], v[34:35] op_sel_hi:[1,0] neg_lo:[0,1] neg_hi:[0,1]
	v_add_f32_e32 v18, v42, v18
	v_pk_mul_f32 v[44:45], v[26:27], v[26:27]
	v_add_f32_e32 v18, v43, v18
	v_pk_add_f32 v[28:29], v[28:29], v[34:35] op_sel_hi:[1,0] neg_lo:[0,1] neg_hi:[0,1]
	v_add_f32_e32 v18, v44, v18
	v_pk_mul_f32 v[46:47], v[28:29], v[28:29]
	v_add_f32_e32 v18, v45, v18
	v_pk_add_f32 v[30:31], v[30:31], v[34:35] op_sel_hi:[1,0] neg_lo:[0,1] neg_hi:[0,1]
	v_add_f32_e32 v18, v46, v18
	v_pk_mul_f32 v[48:49], v[30:31], v[30:31]
	v_add_f32_e32 v18, v47, v18
	v_pk_add_f32 v[32:33], v[32:33], v[34:35] op_sel_hi:[1,0] neg_lo:[0,1] neg_hi:[0,1]
	v_add_f32_e32 v18, v48, v18
	v_pk_mul_f32 v[54:55], v[32:33], v[32:33]
	v_add_f32_e32 v18, v49, v18
	v_pk_add_f32 v[56:57], v[96:97], v[34:35] op_sel_hi:[1,0] neg_lo:[0,1] neg_hi:[0,1]
	v_add_f32_e32 v18, v54, v18
	v_pk_mul_f32 v[58:59], v[56:57], v[56:57]
	v_add_f32_e32 v18, v55, v18
	v_pk_add_f32 v[60:61], v[94:95], v[34:35] op_sel_hi:[1,0] neg_lo:[0,1] neg_hi:[0,1]
	v_add_f32_e32 v18, v58, v18
	v_pk_mul_f32 v[62:63], v[60:61], v[60:61]
	v_add_f32_e32 v18, v59, v18
	v_pk_add_f32 v[64:65], v[6:7], v[34:35] op_sel_hi:[1,0] neg_lo:[0,1] neg_hi:[0,1]
	v_add_f32_e32 v18, v62, v18
	v_pk_mul_f32 v[6:7], v[64:65], v[64:65]
	v_add_f32_e32 v18, v63, v18
	v_pk_add_f32 v[66:67], v[8:9], v[34:35] op_sel_hi:[1,0] neg_lo:[0,1] neg_hi:[0,1]
	v_add_f32_e32 v6, v6, v18
	v_pk_mul_f32 v[8:9], v[66:67], v[66:67]
	v_add_f32_e32 v6, v7, v6
	v_pk_add_f32 v[68:69], v[10:11], v[34:35] op_sel_hi:[1,0] neg_lo:[0,1] neg_hi:[0,1]
	v_add_f32_e32 v6, v8, v6
	v_pk_mul_f32 v[10:11], v[68:69], v[68:69]
	v_add_f32_e32 v6, v9, v6
	v_pk_add_f32 v[70:71], v[12:13], v[34:35] op_sel_hi:[1,0] neg_lo:[0,1] neg_hi:[0,1]
	v_add_f32_e32 v6, v10, v6
	v_pk_mul_f32 v[12:13], v[70:71], v[70:71]
	v_add_f32_e32 v6, v11, v6
	v_pk_add_f32 v[72:73], v[14:15], v[34:35] op_sel_hi:[1,0] neg_lo:[0,1] neg_hi:[0,1]
	v_add_f32_e32 v6, v12, v6
	v_pk_mul_f32 v[14:15], v[72:73], v[72:73]
	v_add_f32_e32 v6, v13, v6
	v_pk_add_f32 v[34:35], v[16:17], v[34:35] op_sel_hi:[1,0] neg_lo:[0,1] neg_hi:[0,1]
	v_add_f32_e32 v6, v14, v6
	v_pk_mul_f32 v[16:17], v[34:35], v[34:35]
	v_add_f32_e32 v6, v15, v6
	v_add_f32_e32 v6, v16, v6
	v_add_f32_e32 v6, v17, v6
	v_mov_b32_e32 v7, v6
	v_mov_b32_e32 v8, v6
	s_nop 1
	v_permlane32_swap_b32_e32 v7, v8
	v_cndmask_b32_e64 v7, v7, v8, s[2:3]
	v_add_f32_e32 v6, v6, v7
	v_mov_b32_e32 v7, 0x3727c5ac
	v_fmac_f32_e32 v7, 0x3c800000, v6
	v_rsq_f32_e32 v40, v7
	ds_read_b128 v[2:5], v173 offset:15104
	ds_read_b128 v[50:53], v173 offset:15392
	ds_read_b128 v[186:189], v173 offset:17408
	ds_read_b128 v[190:193], v173 offset:17696
	ds_read_b128 v[6:9], v173 offset:15680
	ds_read_b128 v[10:13], v173 offset:15968
	ds_read_b128 v[14:17], v173 offset:17984
	ds_read_b128 v[18:21], v173 offset:18272
	s_load_dwordx2 s[0:1], s[0:1], 0x80
	v_pk_mul_f32 v[22:23], v[22:23], v[40:41] op_sel_hi:[1,0]
	v_pk_mul_f32 v[36:37], v[36:37], v[40:41] op_sel_hi:[1,0]
	s_waitcnt lgkmcnt(0)
	v_pk_fma_f32 v[82:83], v[102:103], v[22:23], v[110:111]
	v_pk_mul_f32 v[22:23], v[24:25], v[40:41] op_sel_hi:[1,0]
	v_pk_fma_f32 v[74:75], v[98:99], v[36:37], v[106:107]
	v_pk_fma_f32 v[84:85], v[104:105], v[22:23], v[112:113]
	v_pk_mul_f32 v[22:23], v[26:27], v[40:41] op_sel_hi:[1,0]
	v_pk_mul_f32 v[36:37], v[38:39], v[40:41] op_sel_hi:[1,0]
	v_pk_fma_f32 v[86:87], v[114:115], v[22:23], v[178:179]
	v_pk_mul_f32 v[22:23], v[28:29], v[40:41] op_sel_hi:[1,0]
	v_pk_fma_f32 v[76:77], v[100:101], v[36:37], v[108:109]
	v_pk_fma_f32 v[88:89], v[116:117], v[22:23], v[180:181]
	v_pk_mul_f32 v[22:23], v[30:31], v[40:41] op_sel_hi:[1,0]
	s_nop 0
	v_pk_fma_f32 v[94:95], v[174:175], v[22:23], v[182:183]
	v_pk_mul_f32 v[22:23], v[32:33], v[40:41] op_sel_hi:[1,0]
	s_nop 0
	v_pk_fma_f32 v[110:111], v[176:177], v[22:23], v[184:185]
	v_pk_mul_f32 v[22:23], v[56:57], v[40:41] op_sel_hi:[1,0]
	s_nop 0
	v_pk_fma_f32 v[108:109], v[2:3], v[22:23], v[186:187]
	v_pk_mul_f32 v[2:3], v[60:61], v[40:41] op_sel_hi:[1,0]
	s_nop 0
	v_pk_fma_f32 v[106:107], v[4:5], v[2:3], v[188:189]
	v_pk_mul_f32 v[2:3], v[64:65], v[40:41] op_sel_hi:[1,0]
	s_nop 0
	v_pk_fma_f32 v[104:105], v[50:51], v[2:3], v[190:191]
	v_pk_mul_f32 v[2:3], v[66:67], v[40:41] op_sel_hi:[1,0]
	s_nop 0
	v_pk_fma_f32 v[100:101], v[52:53], v[2:3], v[192:193]
	v_pk_mul_f32 v[2:3], v[68:69], v[40:41] op_sel_hi:[1,0]
	s_nop 0
	v_pk_fma_f32 v[96:97], v[6:7], v[2:3], v[14:15]
	v_pk_mul_f32 v[2:3], v[70:71], v[40:41] op_sel_hi:[1,0]
	s_nop 0
	v_pk_fma_f32 v[92:93], v[8:9], v[2:3], v[16:17]
	v_pk_mul_f32 v[2:3], v[72:73], v[40:41] op_sel_hi:[1,0]
	s_nop 0
	v_pk_fma_f32 v[90:91], v[10:11], v[2:3], v[18:19]
	v_pk_mul_f32 v[2:3], v[34:35], v[40:41] op_sel_hi:[1,0]
	s_nop 0
	v_pk_fma_f32 v[102:103], v[12:13], v[2:3], v[20:21]
	v_lshl_add_u64 v[2:3], v[118:119], 1, s[0:1]
	v_lshlrev_b32_e32 v98, 1, v126
	v_mov_b32_e32 v99, 0
	v_lshl_add_u64 v[2:3], v[2:3], 0, v[98:99]
	v_mbcnt_lo_u32_b32 v254, -1, 0
	v_mbcnt_hi_u32_b32 v254, -1, v254
	v_and_b32_e32 v254, 32, v254
	v_lshrrev_b32_e32 v254, 2, v254
	v_mov_b32_e32 v255, 0
	v_lshl_add_u64 v[254:255], v[2:3], 0, v[254:255]
	v_cvt_pk_f16_f32 v247, v76, v77
	v_cvt_pk_f16_f32 v246, v74, v75
	s_waitcnt vmcnt(0)
	s_barrier
	v_cvt_pk_f16_f32 v249, v84, v85
	v_cvt_pk_f16_f32 v248, v82, v83
	s_nop 1
	v_permlane32_swap_b32_e32 v246, v248
	v_permlane32_swap_b32_e32 v247, v249
	global_store_dwordx4 v[254:255], v[246:249], off
	v_cvt_pk_f16_f32 v251, v88, v89
	v_cvt_pk_f16_f32 v250, v86, v87
	v_cvt_pk_f16_f32 v253, v110, v111
	v_cvt_pk_f16_f32 v252, v94, v95
	s_nop 1
	v_permlane32_swap_b32_e32 v250, v252
	v_permlane32_swap_b32_e32 v251, v253
	global_store_dwordx4 v[254:255], v[250:253], off offset:32
	v_cvt_pk_f16_f32 v247, v106, v107
	v_cvt_pk_f16_f32 v246, v108, v109
	v_cvt_pk_f16_f32 v249, v100, v101
	v_cvt_pk_f16_f32 v248, v104, v105
	s_nop 1
	v_permlane32_swap_b32_e32 v246, v248
	v_permlane32_swap_b32_e32 v247, v249
	global_store_dwordx4 v[254:255], v[246:249], off offset:64
	v_cvt_pk_f16_f32 v251, v92, v93
	v_cvt_pk_f16_f32 v250, v96, v97
	v_cvt_pk_f16_f32 v253, v102, v103
	v_cvt_pk_f16_f32 v252, v90, v91
	s_movk_i32 s0, 0x270
	s_nop 1
	v_permlane32_swap_b32_e32 v250, v252
	v_permlane32_swap_b32_e32 v251, v253
	global_store_dwordx4 v[254:255], v[250:253], off offset:96
	v_cmp_gt_u32_e32 vcc, s0, v0
	v_lshl_add_u32 v2, v0, 2, 0
	s_and_saveexec_b64 s[0:1], vcc
	ds_write_b32 v2, v159 offset:61440
	s_or_b64 exec, exec, s[0:1]
	s_movk_i32 s0, 0x70
	v_cmp_gt_u32_e32 vcc, s0, v0
	s_and_saveexec_b64 s[0:1], vcc
	ds_write_b32 v2, v161 offset:63488
	s_or_b64 exec, exec, s[0:1]
	s_cmpk_lt_u32 s14, 0x900
	s_cbranch_scc0 .LBB2_93
	s_lshl_b32 s0, s22, 10
	s_add_i32 s15, s22, -8
	s_add_i32 s0, s0, 0
	s_add_i32 s18, s0, 0x6000
	s_lshl_b64 s[0:1], s[14:15], 4
	s_and_b32 s1, s1, 15
	s_and_b32 s0, s0, 0xfffffc00
	s_add_u32 s0, s16, s0
	s_addc_u32 s1, s17, s1
	v_lshl_add_u64 v[2:3], v[120:121], 1, s[0:1]
	s_mov_b64 s[0:1], 0x36000
	v_lshl_add_u64 v[2:3], v[2:3], 0, s[0:1]
	s_mov_b64 s[0:1], 0x2000

.LBB2_93:
	ds_read_b128 v[18:21], v125 offset:8192
	ds_read_b128 v[34:37], v125 offset:9216
	v_cvt_pkrtz_f16_f32 v50, v74, v75
	v_cvt_pkrtz_f16_f32 v51, v76, v77
	v_cvt_pkrtz_f16_f32 v52, v82, v83
	v_cvt_pkrtz_f16_f32 v53, v84, v85
	v_cvt_pkrtz_f16_f32 v62, v86, v87
	v_cvt_pkrtz_f16_f32 v63, v88, v89
	v_cvt_pkrtz_f16_f32 v64, v94, v95
	s_waitcnt lgkmcnt(0)
	v_mfma_f32_32x32x16_f16 v[18:33], v[18:21], v[50:53], 0
	v_cvt_pkrtz_f16_f32 v65, v110, v111
	ds_read_b128 v[38:41], v125 offset:10240
	v_cvt_pkrtz_f16_f32 v78, v108, v109
	v_cvt_pkrtz_f16_f32 v79, v106, v107
	v_cvt_pkrtz_f16_f32 v80, v104, v105
	v_cvt_pkrtz_f16_f32 v81, v100, v101
	s_add_i32 s0, 0, 0x1a800
	v_mfma_f32_32x32x16_f16 v[18:33], v[34:37], v[62:65], v[18:33]
	v_lshl_add_u32 v99, v165, 1, s0
	ds_read_b128 v[2:5], v125
	ds_read_b128 v[58:61], v125 offset:1024
	ds_read_b128 v[120:123], v125 offset:2048
	ds_read_b128 v[174:177], v125 offset:3072
	ds_read_b128 v[178:181], v125 offset:4096
	ds_read_b128 v[182:185], v125 offset:5120
	ds_read_b128 v[34:37], v125 offset:11264
	ds_read_b128 v[186:189], v125 offset:6144
	ds_read_b128 v[190:193], v125 offset:7168
	v_cvt_pkrtz_f16_f32 v114, v96, v97
	v_cvt_pkrtz_f16_f32 v115, v92, v93
	s_waitcnt lgkmcnt(0)
	v_mfma_f32_32x32x16_f16 v[18:33], v[38:41], v[78:81], v[18:33]
	ds_read_b128 v[194:197], v99 offset:11648
	ds_read_b128 v[198:201], v99 offset:11936
	ds_read_b128 v[38:41], v125 offset:12288
	v_cvt_pkrtz_f16_f32 v116, v90, v91
	v_cvt_pkrtz_f16_f32 v117, v102, v103
	ds_read_b128 v[202:205], v99 offset:12224
	ds_read_b128 v[206:209], v99 offset:12512
	ds_read_b128 v[210:213], v99 offset:12800
	ds_read_b128 v[54:57], v99 offset:13088
	ds_read_b128 v[70:73], v99 offset:13376
	ds_read_b128 v[66:69], v99 offset:13664
	ds_read_b128 v[214:217], v125 offset:13312
	ds_read_b128 v[218:221], v99 offset:13952
	ds_read_b128 v[222:225], v125 offset:14336
	ds_read_b128 v[226:229], v125 offset:15360
	ds_read_b128 v[230:233], v99 offset:14240
	s_mov_b32 s16, 0xff61b1e6
	s_mov_b32 s17, 0
	v_mfma_f32_32x32x16_f16 v[18:33], v[34:37], v[114:117], v[18:33]
	s_waitcnt lgkmcnt(0)
	v_mfma_f32_32x32x16_f16 v[34:49], v[38:41], v[50:53], 0
	s_nop 9
	v_add_f32_e32 v112, v18, v218
	v_add_f32_e32 v113, v19, v219
	v_add_f32_e32 v159, v20, v220
	v_add_f32_e32 v161, v21, v221
	ds_read_b128 v[18:21], v99 offset:14528
	v_add_f32_e32 v164, v22, v230
	v_add_f32_e32 v165, v23, v231
	v_mfma_f32_32x32x16_f16 v[34:49], v[214:217], v[62:65], v[34:49]
	v_add_f32_e32 v170, v24, v232
	v_add_f32_e32 v173, v25, v233
	ds_read_b128 v[22:25], v99 offset:14816
	s_waitcnt lgkmcnt(0)
	v_add_f32_e32 v26, v26, v18
	v_add_f32_e32 v27, v27, v19
	v_add_f32_e32 v28, v28, v20
	v_add_f32_e32 v29, v29, v21
	v_mfma_f32_32x32x16_f16 v[34:49], v[222:225], v[78:81], v[34:49]
	ds_read_b128 v[18:21], v99 offset:15104
	v_add_f32_e32 v30, v30, v22
	v_add_f32_e32 v31, v31, v23
	v_add_f32_e32 v32, v32, v24
	v_add_f32_e32 v33, v33, v25
	ds_read_b128 v[22:25], v99 offset:15392
	v_mfma_f32_32x32x16_f16 v[34:49], v[226:229], v[114:117], v[34:49]
	v_mfma_f32_32x32x16_f16 v[2:17], v[2:5], v[50:53], 0
	s_waitcnt lgkmcnt(0)
	s_nop 9
	v_add_f32_e32 v34, v34, v18
	v_add_f32_e32 v35, v35, v19
	v_add_f32_e32 v36, v36, v20
	v_add_f32_e32 v37, v37, v21
	ds_read_b128 v[18:21], v99 offset:15680
	v_add_f32_e32 v38, v38, v22
	v_add_f32_e32 v39, v39, v23
	v_add_f32_e32 v40, v40, v24
	v_add_f32_e32 v41, v41, v25
	ds_read_b128 v[22:25], v99 offset:15968
	s_waitcnt lgkmcnt(0)
	v_add_f32_e32 v42, v42, v18
	v_add_f32_e32 v43, v43, v19
	v_add_f32_e32 v44, v44, v20
	v_add_f32_e32 v45, v45, v21
	v_cvt_pkrtz_f16_f32 v18, v112, v113
	v_cvt_pkrtz_f16_f32 v19, v159, v161
	v_cvt_pkrtz_f16_f32 v20, v164, v165
	v_cvt_pkrtz_f16_f32 v21, v170, v173
	ds_write_b128 v166, v[18:21]
	v_cvt_pkrtz_f16_f32 v18, v26, v27
	v_cvt_pkrtz_f16_f32 v19, v28, v29
	v_cvt_pkrtz_f16_f32 v20, v30, v31
	v_cvt_pkrtz_f16_f32 v21, v32, v33
	v_add_f32_e32 v22, v46, v22
	v_add_f32_e32 v23, v47, v23
	v_add_f32_e32 v24, v48, v24
	v_add_f32_e32 v25, v49, v25
	ds_write_b128 v166, v[18:21] offset:32
	v_cvt_pkrtz_f16_f32 v18, v34, v35
	v_cvt_pkrtz_f16_f32 v19, v36, v37
	v_cvt_pkrtz_f16_f32 v20, v38, v39
	v_cvt_pkrtz_f16_f32 v21, v40, v41
	ds_write_b128 v166, v[18:21] offset:64
	v_cvt_pkrtz_f16_f32 v18, v42, v43
	v_cvt_pkrtz_f16_f32 v19, v44, v45
	v_cvt_pkrtz_f16_f32 v20, v22, v23
	v_cvt_pkrtz_f16_f32 v21, v24, v25
	ds_write_b128 v166, v[18:21] offset:96
	ds_read_b128 v[18:21], v125 offset:16384
	ds_read_b128 v[22:25], v125 offset:17408
	s_waitcnt lgkmcnt(0)
	v_mfma_f32_32x32x16_f16 v[30:45], v[50:53], v[18:21], 0
	v_add_u32_e32 v112, v167, v162
	v_add_u32_e32 v159, v171, v172
	v_mfma_f32_32x32x16_f16 v[2:17], v[58:61], v[62:65], v[2:17]
	v_mfma_f32_32x32x16_f16 v[30:45], v[62:65], v[22:25], v[30:45]
	ds_read_b128 v[18:21], v125 offset:18432
	ds_read_b128 v[22:25], v125 offset:19456
	v_mfma_f32_32x32x16_f16 v[2:17], v[120:123], v[78:81], v[2:17]
	s_waitcnt lgkmcnt(0)
	v_mfma_f32_32x32x16_f16 v[30:45], v[78:81], v[18:21], v[30:45]
	v_add3_u32 v18, s0, v168, v160
	ds_read_b32 v46, v18 offset:16256
	v_mfma_f32_32x32x16_f16 v[2:17], v[174:177], v[114:117], v[2:17]
	v_mfma_f32_32x32x16_f16 v[30:45], v[114:117], v[22:25], v[30:45]
	s_nop 10
	v_fmamk_f32 v58, v194, 0x3e38aa3b, v2
	v_fmamk_f32 v59, v195, 0x3e38aa3b, v3
	v_fmamk_f32 v99, v198, 0x3e38aa3b, v6
	v_fmamk_f32 v113, v202, 0x3e38aa3b, v10
	v_fmamk_f32 v120, v203, 0x3e38aa3b, v11
	v_fmamk_f32 v121, v204, 0x3e38aa3b, v12
	v_fmamk_f32 v122, v205, 0x3e38aa3b, v13
	s_waitcnt lgkmcnt(0)
	v_add_f32_e32 v2, v46, v30
	v_add_f32_e32 v3, v46, v31
	v_add_f32_e32 v47, v46, v32
	v_add_f32_e32 v48, v46, v33
	v_add_f32_e32 v49, v46, v34
	v_add_f32_e32 v60, v46, v35
	v_add_f32_e32 v61, v46, v36
	v_add_f32_e32 v37, v46, v37
	v_add_f32_e32 v38, v46, v38
	v_add_f32_e32 v39, v46, v39
	v_add_f32_e32 v40, v46, v40
	v_add_f32_e32 v41, v46, v41
	v_add_f32_e32 v42, v46, v42
	v_add_f32_e32 v43, v46, v43
	v_add_f32_e32 v44, v46, v44
	v_add_f32_e32 v45, v46, v45
	v_cvt_pkrtz_f16_f32 v34, v2, v3
	v_cvt_pkrtz_f16_f32 v35, v47, v48
	v_cvt_pkrtz_f16_f32 v36, v49, v60
	v_cvt_pkrtz_f16_f32 v37, v61, v37
	ds_write_b128 v112, v[34:37]
	v_cvt_pkrtz_f16_f32 v34, v38, v39
	v_cvt_pkrtz_f16_f32 v35, v40, v41
	v_cvt_pkrtz_f16_f32 v36, v42, v43
	v_cvt_pkrtz_f16_f32 v37, v44, v45
	ds_write_b128 v112, v[34:37] offset:32
	ds_read_b128 v[34:37], v125 offset:20480
	v_fmamk_f32 v60, v196, 0x3e38aa3b, v4
	v_fmamk_f32 v61, v197, 0x3e38aa3b, v5
	ds_read_b128 v[2:5], v125 offset:21504
	s_waitcnt lgkmcnt(0)
	v_mfma_f32_32x32x16_f16 v[34:49], v[50:53], v[34:37], 0
	v_fmamk_f32 v14, v206, 0x3e38aa3b, v14
	v_fmamk_f32 v15, v207, 0x3e38aa3b, v15
	v_fmamk_f32 v16, v208, 0x3e38aa3b, v16
	v_fmac_f32_e32 v17, 0x3e38aa3b, v209
	v_mfma_f32_32x32x16_f16 v[34:49], v[62:65], v[2:5], v[34:49]
	ds_read_b128 v[2:5], v125 offset:22528
	v_mfma_f32_32x32x16_f16 v[18:33], v[178:181], v[50:53], 0
	v_fmamk_f32 v50, v199, 0x3e38aa3b, v7
	v_fmamk_f32 v51, v200, 0x3e38aa3b, v8
	v_fmamk_f32 v52, v201, 0x3e38aa3b, v9
	ds_read_b128 v[6:9], v125 offset:23552
	s_waitcnt lgkmcnt(0)
	v_mfma_f32_32x32x16_f16 v[34:49], v[78:81], v[2:5], v[34:49]
	v_add3_u32 v2, s0, v169, v160
	ds_read_b32 v2, v2 offset:16256
	s_lshl_b32 s0, s28, 9
	s_add_i32 s0, s0, 0
	s_add_i32 s14, s0, 0x27800
	v_mfma_f32_32x32x16_f16 v[18:33], v[182:185], v[62:65], v[18:33]
	v_mfma_f32_32x32x16_f16 v[34:49], v[114:117], v[6:9], v[34:49]
	v_mfma_f32_32x32x16_f16 v[18:33], v[186:189], v[78:81], v[18:33]
	s_waitcnt lgkmcnt(0)
	s_nop 9
	v_add_f32_e32 v3, v2, v34
	v_add_f32_e32 v4, v2, v35
	v_add_f32_e32 v5, v2, v36
	v_add_f32_e32 v6, v2, v37
	v_add_f32_e32 v7, v2, v38
	v_add_f32_e32 v8, v2, v39
	v_add_f32_e32 v9, v2, v40
	v_add_f32_e32 v10, v2, v41
	v_add_f32_e32 v11, v2, v42
	v_add_f32_e32 v12, v2, v43
	v_add_f32_e32 v13, v2, v44
	v_add_f32_e32 v34, v2, v45
	v_add_f32_e32 v35, v2, v46
	v_add_f32_e32 v36, v2, v47
	v_add_f32_e32 v37, v2, v48
	v_add_f32_e32 v38, v2, v49
	v_cvt_pkrtz_f16_f32 v2, v3, v4
	v_cvt_pkrtz_f16_f32 v3, v5, v6
	v_cvt_pkrtz_f16_f32 v4, v7, v8
	v_cvt_pkrtz_f16_f32 v5, v9, v10
	ds_write_b128 v112, v[2:5] offset:8704
	v_cvt_pkrtz_f16_f32 v2, v11, v12
	v_cvt_pkrtz_f16_f32 v3, v13, v34
	v_cvt_pkrtz_f16_f32 v4, v35, v36
	v_cvt_pkrtz_f16_f32 v5, v37, v38
	ds_write_b128 v112, v[2:5] offset:8736
	s_nop 0
	s_waitcnt lgkmcnt(0)
	s_barrier
	ds_read_b128 v[2:5], v159
	ds_read_b128 v[10:13], v159 offset:32
	v_mfma_f32_32x32x16_f16 v[18:33], v[190:193], v[114:117], v[18:33]
	v_cvt_pkrtz_f16_f32 v6, v58, v59
	v_cvt_pkrtz_f16_f32 v7, v60, v61
	v_cvt_pkrtz_f16_f32 v8, v99, v50
	v_cvt_pkrtz_f16_f32 v9, v51, v52
	v_cvt_pkrtz_f16_f32 v78, v113, v120
	v_cvt_pkrtz_f16_f32 v79, v121, v122
	v_cvt_pkrtz_f16_f32 v80, v14, v15
	s_nop 4
	v_fmamk_f32 v22, v54, 0x3e38aa3b, v22
	v_fmamk_f32 v23, v55, 0x3e38aa3b, v23
	v_fmamk_f32 v24, v56, 0x3e38aa3b, v24
	v_fmamk_f32 v25, v57, 0x3e38aa3b, v25
	s_waitcnt lgkmcnt(1)
	v_mfma_f32_32x32x16_f16 v[50:65], v[2:5], v[6:9], 0
	v_cvt_pkrtz_f16_f32 v81, v16, v17
	ds_read_b128 v[2:5], v159 offset:64
	v_fmamk_f32 v18, v210, 0x3e38aa3b, v18
	v_fmamk_f32 v19, v211, 0x3e38aa3b, v19
	v_fmamk_f32 v20, v212, 0x3e38aa3b, v20
	v_fmamk_f32 v21, v213, 0x3e38aa3b, v21
	v_fmamk_f32 v26, v70, 0x3e38aa3b, v26
	s_waitcnt lgkmcnt(1)
	v_mfma_f32_32x32x16_f16 v[50:65], v[10:13], v[78:81], v[50:65]
	v_fmamk_f32 v27, v71, 0x3e38aa3b, v27
	v_fmamk_f32 v28, v72, 0x3e38aa3b, v28
	v_fmamk_f32 v14, v73, 0x3e38aa3b, v29
	v_cvt_pkrtz_f16_f32 v70, v18, v19
	v_cvt_pkrtz_f16_f32 v71, v20, v21
	v_cvt_pkrtz_f16_f32 v72, v22, v23
	v_cvt_pkrtz_f16_f32 v73, v24, v25
	ds_read_b128 v[10:13], v159 offset:96
	v_fmamk_f32 v15, v66, 0x3e38aa3b, v30
	s_waitcnt lgkmcnt(1)
	v_mfma_f32_32x32x16_f16 v[50:65], v[2:5], v[70:73], v[50:65]
	v_fmamk_f32 v2, v67, 0x3e38aa3b, v31
	v_fmamk_f32 v3, v68, 0x3e38aa3b, v32
	v_fmac_f32_e32 v33, 0x3e38aa3b, v69
	v_cvt_pkrtz_f16_f32 v66, v26, v27
	v_cvt_pkrtz_f16_f32 v67, v28, v14
	v_cvt_pkrtz_f16_f32 v68, v15, v2
	v_cvt_pkrtz_f16_f32 v69, v3, v33
	v_add_u32_e32 v113, v163, v162
	s_waitcnt lgkmcnt(0)
	v_mfma_f32_32x32x16_f16 v[50:65], v[10:13], v[66:69], v[50:65]
	ds_read_b128 v[2:5], v159 offset:4608
	ds_read_b128 v[10:13], v159 offset:4640
	s_waitcnt lgkmcnt(1)
	v_mfma_f32_32x32x16_f16 v[34:49], v[2:5], v[6:9], 0
	s_waitcnt lgkmcnt(0)
	v_mfma_f32_32x32x16_f16 v[34:49], v[10:13], v[78:81], v[34:49]
	ds_read_b128 v[2:5], v159 offset:4672
	ds_read_b128 v[10:13], v159 offset:4704
	s_waitcnt lgkmcnt(1)
	v_mfma_f32_32x32x16_f16 v[34:49], v[2:5], v[70:73], v[34:49]
	s_waitcnt lgkmcnt(0)
	v_mfma_f32_32x32x16_f16 v[34:49], v[10:13], v[66:69], v[34:49]
	ds_read_b128 v[2:5], v159 offset:9216
	ds_read_b128 v[10:13], v159 offset:9248
	s_waitcnt lgkmcnt(1)
	v_mfma_f32_32x32x16_f16 v[18:33], v[2:5], v[6:9], 0
	s_waitcnt lgkmcnt(0)
	v_mfma_f32_32x32x16_f16 v[18:33], v[10:13], v[78:81], v[18:33]
	ds_read_b128 v[2:5], v159 offset:9280
	ds_read_b128 v[10:13], v159 offset:9312
	s_waitcnt lgkmcnt(1)
	v_mfma_f32_32x32x16_f16 v[18:33], v[2:5], v[70:73], v[18:33]
	ds_read_b128 v[2:5], v159 offset:13824
	ds_read_b128 v[114:117], v159 offset:13856
	ds_read_b128 v[120:123], v159 offset:13888
	ds_read_b128 v[164:167], v159 offset:13920
	s_waitcnt lgkmcnt(4)
	v_mfma_f32_32x32x16_f16 v[18:33], v[10:13], v[66:69], v[18:33]
	s_waitcnt lgkmcnt(3)
	v_mfma_f32_32x32x16_f16 v[2:17], v[2:5], v[6:9], 0
	s_waitcnt lgkmcnt(2)
	v_mfma_f32_32x32x16_f16 v[2:17], v[114:117], v[78:81], v[2:17]
	s_waitcnt lgkmcnt(1)
	v_mfma_f32_32x32x16_f16 v[2:17], v[120:123], v[70:73], v[2:17]
	s_waitcnt lgkmcnt(0)
	v_mfma_f32_32x32x16_f16 v[2:17], v[164:167], v[66:69], v[2:17]
	v_mov_b32_e32 v99, 0
	s_nop 10
	s_nop 1
	v_exp_f32_e32 v34, v34
	v_exp_f32_e32 v35, v35
	v_exp_f32_e32 v36, v36
	v_exp_f32_e32 v37, v37
	v_cvt_pkrtz_f16_f32 v34, v34, v35
	v_cvt_pkrtz_f16_f32 v35, v36, v37
	v_exp_f32_e32 v36, v38
	v_exp_f32_e32 v37, v39
	v_exp_f32_e32 v38, v40
	v_exp_f32_e32 v39, v41
	v_exp_f32_e32 v40, v42
	v_exp_f32_e32 v41, v43
	v_exp_f32_e32 v42, v44
	v_exp_f32_e32 v43, v45
	v_cvt_pkrtz_f16_f32 v36, v36, v37
	v_cvt_pkrtz_f16_f32 v37, v38, v39
	v_cvt_pkrtz_f16_f32 v38, v40, v41
	v_cvt_pkrtz_f16_f32 v39, v42, v43
	v_exp_f32_e32 v40, v46
	v_exp_f32_e32 v41, v47
	v_exp_f32_e32 v42, v48
	v_exp_f32_e32 v43, v49
	v_exp_f32_e32 v18, v18
	v_exp_f32_e32 v19, v19
	v_exp_f32_e32 v20, v20
	v_exp_f32_e32 v21, v21
	v_exp_f32_e32 v50, v50
	v_exp_f32_e32 v51, v51
	v_exp_f32_e32 v52, v52
	v_exp_f32_e32 v53, v53
	v_cvt_pkrtz_f16_f32 v40, v40, v41
	v_cvt_pkrtz_f16_f32 v41, v42, v43
	v_cvt_pkrtz_f16_f32 v42, v18, v19
	v_cvt_pkrtz_f16_f32 v43, v20, v21
	v_exp_f32_e32 v18, v22
	v_exp_f32_e32 v19, v23
	v_exp_f32_e32 v20, v24
	v_exp_f32_e32 v21, v25
	v_cvt_pkrtz_f16_f32 v50, v50, v51
	v_cvt_pkrtz_f16_f32 v51, v52, v53
	v_exp_f32_e32 v52, v54
	v_exp_f32_e32 v53, v55
	v_exp_f32_e32 v54, v56
	v_exp_f32_e32 v55, v57
	v_exp_f32_e32 v56, v58
	v_exp_f32_e32 v57, v59
	v_exp_f32_e32 v58, v60
	v_exp_f32_e32 v59, v61
	v_cvt_pkrtz_f16_f32 v44, v18, v19
	v_cvt_pkrtz_f16_f32 v45, v20, v21
	ds_read_b128 v[18:21], v113
	v_exp_f32_e32 v22, v26
	v_exp_f32_e32 v23, v27
	v_cvt_pkrtz_f16_f32 v52, v52, v53
	v_cvt_pkrtz_f16_f32 v53, v54, v55
	v_cvt_pkrtz_f16_f32 v54, v56, v57
	v_cvt_pkrtz_f16_f32 v55, v58, v59
	v_exp_f32_e32 v56, v62
	v_exp_f32_e32 v57, v63
	v_exp_f32_e32 v58, v64
	v_exp_f32_e32 v59, v65
	v_exp_f32_e32 v24, v28
	v_exp_f32_e32 v25, v29
	v_cvt_pkrtz_f16_f32 v46, v22, v23
	v_exp_f32_e32 v48, v30
	v_exp_f32_e32 v49, v31
	v_cvt_pkrtz_f16_f32 v56, v56, v57
	v_cvt_pkrtz_f16_f32 v57, v58, v59
	v_exp_f32_e32 v62, v32
	ds_read_b128 v[58:61], v113 offset:32
	v_cvt_pkrtz_f16_f32 v47, v24, v25
	v_exp_f32_e32 v63, v33
	s_waitcnt lgkmcnt(1)
	v_mfma_f32_32x32x16_f16 v[18:33], v[18:21], v[50:53], 0
	v_cvt_pkrtz_f16_f32 v48, v48, v49
	v_cvt_pkrtz_f16_f32 v49, v62, v63
	ds_read_b128 v[62:65], v113 offset:64
	v_exp_f32_e32 v67, v2
	v_exp_f32_e32 v68, v3
	s_waitcnt lgkmcnt(1)
	v_mfma_f32_32x32x16_f16 v[18:33], v[58:61], v[54:57], v[18:33]
	v_exp_f32_e32 v59, v4
	v_exp_f32_e32 v60, v5
	v_exp_f32_e32 v61, v6
	ds_read_b128 v[2:5], v113 offset:96
	s_waitcnt lgkmcnt(1)
	v_mfma_f32_32x32x16_f16 v[18:33], v[62:65], v[34:37], v[18:33]
	v_exp_f32_e32 v62, v7
	v_exp_f32_e32 v63, v8
	v_exp_f32_e32 v64, v9
	ds_read_b128 v[6:9], v113 offset:128
	s_waitcnt lgkmcnt(1)
	v_mfma_f32_32x32x16_f16 v[18:33], v[2:5], v[38:41], v[18:33]
	v_exp_f32_e32 v10, v10
	ds_read_b128 v[2:5], v113 offset:160
	v_cvt_pkrtz_f16_f32 v58, v67, v68
	v_cvt_pkrtz_f16_f32 v59, v59, v60
	v_cvt_pkrtz_f16_f32 v60, v61, v62
	v_cvt_pkrtz_f16_f32 v61, v63, v64
	s_waitcnt lgkmcnt(1)
	v_mfma_f32_32x32x16_f16 v[18:33], v[6:9], v[42:45], v[18:33]
	v_exp_f32_e32 v11, v11
	v_exp_f32_e32 v12, v12
	v_exp_f32_e32 v13, v13
	ds_read_b128 v[6:9], v113 offset:192
	s_waitcnt lgkmcnt(1)
	v_mfma_f32_32x32x16_f16 v[18:33], v[2:5], v[46:49], v[18:33]
	v_exp_f32_e32 v14, v14
	v_exp_f32_e32 v15, v15
	v_exp_f32_e32 v16, v16
	ds_read_b128 v[2:5], v113 offset:224
	s_waitcnt lgkmcnt(1)
	v_mfma_f32_32x32x16_f16 v[18:33], v[6:9], v[58:61], v[18:33]
	v_exp_f32_e32 v6, v17
	v_cvt_pkrtz_f16_f32 v62, v10, v11
	v_cvt_pkrtz_f16_f32 v63, v12, v13
	v_cvt_pkrtz_f16_f32 v64, v14, v15
	v_cvt_pkrtz_f16_f32 v65, v16, v6
	ds_read_b128 v[6:9], v113 offset:8704
	ds_read_b128 v[66:69], v113 offset:8736
	s_waitcnt lgkmcnt(2)
	v_mfma_f32_32x32x16_f16 v[18:33], v[2:5], v[62:65], v[18:33]
	v_mov_b32_e32 v70, 0
	v_dot2c_f32_f16_e32 v70, 0x3c003c00, v50
	v_dot2c_f32_f16_e32 v70, 0x3c003c00, v51
	v_dot2c_f32_f16_e32 v70, 0x3c003c00, v52
	v_dot2c_f32_f16_e32 v70, 0x3c003c00, v53
	v_dot2c_f32_f16_e32 v70, 0x3c003c00, v54
	v_dot2c_f32_f16_e32 v70, 0x3c003c00, v55
	s_waitcnt lgkmcnt(1)
	v_mfma_f32_32x32x16_f16 v[2:17], v[6:9], v[50:53], 0
	ds_read_b128 v[50:53], v113 offset:8768
	v_dot2c_f32_f16_e32 v70, 0x3c003c00, v56
	v_dot2c_f32_f16_e32 v70, 0x3c003c00, v57
	v_dot2c_f32_f16_e32 v70, 0x3c003c00, v34
	v_dot2c_f32_f16_e32 v70, 0x3c003c00, v35
	v_dot2c_f32_f16_e32 v70, 0x3c003c00, v36
	v_dot2c_f32_f16_e32 v70, 0x3c003c00, v37
	s_waitcnt lgkmcnt(1)
	v_mfma_f32_32x32x16_f16 v[2:17], v[66:69], v[54:57], v[2:17]
	ds_read_b128 v[54:57], v113 offset:8800
	v_dot2c_f32_f16_e32 v70, 0x3c003c00, v38
	v_dot2c_f32_f16_e32 v70, 0x3c003c00, v39
	v_dot2c_f32_f16_e32 v70, 0x3c003c00, v40
	v_dot2c_f32_f16_e32 v70, 0x3c003c00, v41
	v_dot2c_f32_f16_e32 v70, 0x3c003c00, v42
	v_dot2c_f32_f16_e32 v70, 0x3c003c00, v43
	s_waitcnt lgkmcnt(1)
	v_mfma_f32_32x32x16_f16 v[2:17], v[50:53], v[34:37], v[2:17]
	v_dot2c_f32_f16_e32 v70, 0x3c003c00, v44
	ds_read_b128 v[34:37], v113 offset:8832
	v_dot2c_f32_f16_e32 v70, 0x3c003c00, v45
	v_dot2c_f32_f16_e32 v70, 0x3c003c00, v46
	v_dot2c_f32_f16_e32 v70, 0x3c003c00, v47
	v_dot2c_f32_f16_e32 v70, 0x3c003c00, v48
	v_dot2c_f32_f16_e32 v70, 0x3c003c00, v49
	s_waitcnt lgkmcnt(1)
	v_mfma_f32_32x32x16_f16 v[2:17], v[54:57], v[38:41], v[2:17]
	v_dot2c_f32_f16_e32 v70, 0x3c003c00, v58
	v_dot2c_f32_f16_e32 v70, 0x3c003c00, v59
	v_dot2c_f32_f16_e32 v70, 0x3c003c00, v60
	ds_read_b128 v[38:41], v113 offset:8864
	v_dot2c_f32_f16_e32 v70, 0x3c003c00, v61
	v_dot2c_f32_f16_e32 v70, 0x3c003c00, v62
	v_dot2c_f32_f16_e32 v70, 0x3c003c00, v63
	s_waitcnt lgkmcnt(1)
	v_mfma_f32_32x32x16_f16 v[2:17], v[34:37], v[42:45], v[2:17]
	v_dot2c_f32_f16_e32 v70, 0x3c003c00, v64
	v_dot2c_f32_f16_e32 v70, 0x3c003c00, v65
	s_nop 2
	v_mov_b32_e32 v34, v70
	v_mov_b32_e32 v35, v70
	s_nop 1
	v_permlane32_swap_b32_e32 v34, v35
	v_cndmask_b32_e64 v42, v34, v35, s[2:3]
	ds_read_b128 v[34:37], v113 offset:8896
	s_waitcnt lgkmcnt(1)
	v_mfma_f32_32x32x16_f16 v[2:17], v[38:41], v[46:49], v[2:17]
	v_add_f32_e32 v38, v70, v42
	v_rcp_f32_e32 v42, v38
	ds_read_b128 v[38:41], v113 offset:8928
	v_fma_f32 v78, v42, v18, v74
	v_fma_f32 v79, v42, v19, v75
	v_fma_f32 v80, v42, v20, v76
	v_fma_f32 v81, v42, v21, v77
	s_waitcnt lgkmcnt(1)
	v_mfma_f32_32x32x16_f16 v[2:17], v[34:37], v[58:61], v[2:17]
	v_fma_f32 v82, v42, v22, v82
	v_fma_f32 v83, v42, v23, v83
	v_fma_f32 v84, v42, v24, v84
	v_fma_f32 v85, v42, v25, v85
	v_fma_f32 v86, v42, v26, v86
	v_fma_f32 v87, v42, v27, v87
	v_fma_f32 v88, v42, v28, v88
	v_fma_f32 v89, v42, v29, v89
	v_fma_f32 v72, v42, v30, v94
	v_fma_f32 v73, v42, v31, v95
	v_fma_f32 v74, v42, v32, v110
	v_fma_f32 v75, v42, v33, v111
	s_waitcnt lgkmcnt(0)
	v_mfma_f32_32x32x16_f16 v[2:17], v[38:41], v[62:65], v[2:17]
	s_nop 11
	v_fma_f32 v76, v42, v2, v108
	v_fma_f32 v77, v42, v3, v109
	v_fma_f32 v68, v42, v4, v106
	v_fma_f32 v69, v42, v5, v107
	v_fma_f32 v70, v42, v6, v104
	v_fma_f32 v71, v42, v7, v105
	v_pk_fma_f32 v[58:59], v[42:43], v[8:9], v[100:101] op_sel_hi:[0,1,1]
	v_pk_fma_f32 v[66:67], v[42:43], v[10:11], v[96:97] op_sel_hi:[0,1,1]
	v_pk_fma_f32 v[60:61], v[42:43], v[12:13], v[92:93] op_sel_hi:[0,1,1]
	v_pk_fma_f32 v[62:63], v[42:43], v[14:15], v[90:91] op_sel_hi:[0,1,1]
	v_pk_fma_f32 v[64:65], v[42:43], v[16:17], v[102:103] op_sel_hi:[0,1,1]
	v_lshl_add_u64 v[2:3], v[118:119], 1, s[4:5]
	v_lshl_add_u64 v[2:3], v[2:3], 0, v[98:99]
	v_mbcnt_lo_u32_b32 v254, -1, 0
	v_mbcnt_hi_u32_b32 v254, -1, v254
	v_and_b32_e32 v254, 32, v254
	v_lshrrev_b32_e32 v254, 2, v254
	v_mov_b32_e32 v255, 0
	v_lshl_add_u64 v[254:255], v[2:3], 0, v[254:255]
	v_cvt_pk_f16_f32 v247, v80, v81
	v_cvt_pk_f16_f32 v246, v78, v79
	s_waitcnt vmcnt(0)
	s_barrier
	v_cvt_pk_f16_f32 v249, v84, v85
	v_cvt_pk_f16_f32 v248, v82, v83
	s_nop 1
	v_permlane32_swap_b32_e32 v246, v248
	v_permlane32_swap_b32_e32 v247, v249
	global_store_dwordx4 v[254:255], v[246:249], off
	v_cvt_pk_f16_f32 v251, v88, v89
	v_cvt_pk_f16_f32 v250, v86, v87
	v_cvt_pk_f16_f32 v253, v74, v75
	v_cvt_pk_f16_f32 v252, v72, v73
	s_nop 1
	v_permlane32_swap_b32_e32 v250, v252
	v_permlane32_swap_b32_e32 v251, v253
	global_store_dwordx4 v[254:255], v[250:253], off offset:32
	v_cvt_pk_f16_f32 v247, v68, v69
	v_cvt_pk_f16_f32 v246, v76, v77
	v_cvt_pk_f16_f32 v249, v58, v59
	v_cvt_pk_f16_f32 v248, v70, v71
	s_nop 1
	v_permlane32_swap_b32_e32 v246, v248
	v_permlane32_swap_b32_e32 v247, v249
	global_store_dwordx4 v[254:255], v[246:249], off offset:64
	v_cvt_pk_f16_f32 v251, v60, v61
	v_cvt_pk_f16_f32 v250, v66, v67
	v_cvt_pk_f16_f32 v253, v64, v65
	v_cvt_pk_f16_f32 v252, v62, v63
	v_cmp_gt_u32_e64 s[0:1], 32, v124
	v_lshl_add_u32 v91, v126, 2, s14
	v_lshl_add_u32 v93, v1, 2, s14
	v_mov_b32_e32 v240, 0x3e4ccccd
	v_mov_b32_e32 v241, 0x3e4ccccd
	s_mov_b64 s[4:5], -1
	v_mov_b32_e32 v95, v78
	v_mov_b32_e32 v94, v79
	v_mov_b32_e32 v97, v80
	v_mov_b32_e32 v96, v81
	v_mov_b32_e32 v99, v82
	v_mov_b32_e32 v98, v83
	v_mov_b32_e32 v35, v84
	v_mov_b32_e32 v34, v85
	v_mov_b32_e32 v37, v86
	v_mov_b32_e32 v36, v87
	v_mov_b32_e32 v39, v88
	v_mov_b32_e32 v38, v89
	v_mov_b32_e32 v41, v72
	v_mov_b32_e32 v40, v73
	v_mov_b32_e32 v19, v74
	v_mov_b32_e32 v18, v75
	v_mov_b32_e32 v21, v76
	v_mov_b32_e32 v20, v77
	v_mov_b32_e32 v23, v68
	v_mov_b32_e32 v22, v69
	v_mov_b32_e32 v42, v70
	v_mov_b32_e32 v24, v71
	v_mov_b32_e32 v43, v58
	v_mov_b32_e32 v27, v59
	v_mov_b32_e32 v26, v66
	v_mov_b32_e32 v25, v67
	v_mov_b32_e32 v29, v60
	v_mov_b32_e32 v28, v61
	v_mov_b32_e32 v32, v62
	v_mov_b32_e32 v30, v63
	v_mov_b32_e32 v33, v64
	v_mov_b32_e32 v31, v65
	s_nop 1
	v_permlane32_swap_b32_e32 v250, v252
	v_permlane32_swap_b32_e32 v251, v253
	global_store_dwordx4 v[254:255], v[250:253], off offset:96
	s_branch .LBB2_95
